# baseline (speedup 1.0000x reference)
_Z11k_proj_mfmaPKDF16_PKDv8_DF16_PKfPfPS1_S6_PhS6_PDF16_:
	s_and_b32 s3, s2, 7
	s_lshl_b32 s3, s3, 5
	s_lshr_b32 s2, s2, 3
	s_or_b32 s2, s2, s3
	s_bitcmp1_b32 s2, 2
	s_cbranch_scc0 .Lmy_proj_nosleep
	s_sleep 20
